# out-proj EpiResid epilogue: residual loads pipelined 12 deep with counted vmcnt instead of load-wait-store round trips (on top of NA remap)
# baseline (speedup 1.0000x reference)
.LBB0_1373:
	s_lshl_b32 s22, s78, 8
	s_min_i32 s20, s22, 0x2000
	s_ashr_i32 s20, s20, 11
	v_lshl_or_b32 v130, s76, 8, v156
	s_mul_hi_i32 s21, s20, 0xc000
	s_mul_i32 s20, s20, 0xc000
	s_add_u32 s20, s55, s20
	v_ashrrev_i32_e32 v131, 31, v130
	v_add_u32_e32 v148, s22, v154
	s_addc_u32 s21, s69, s21
	v_lshlrev_b64 v[146:147], 2, v[130:131]
	v_ashrrev_i32_e32 v149, 31, v148
	v_lshl_add_u64 v[130:131], s[20:21], 0, v[146:147]
	v_lshlrev_b64 v[150:151], 13, v[148:149]
	v_add_co_u32_e32 v132, vcc, s62, v130
	v_lshl_add_u64 v[134:135], s[8:9], 0, v[150:151]
	v_add_u32_e32 v96, 0xffffe000, v148
	v_addc_co_u32_e32 v133, vcc, 0, v131, vcc
	v_lshl_add_u64 v[162:163], v[134:135], 0, v[146:147]
	v_lshlrev_b64 v[134:135], 13, v[96:97]
	v_lshl_add_u64 v[136:137], s[10:11], 0, v[150:151]
	v_lshl_add_u64 v[134:135], s[12:13], 0, v[134:135]
	v_cmp_gt_i32_e32 vcc, s53, v148
	s_mov_b64 s[20:21], 0x4000
	v_lshl_add_u64 v[130:131], v[130:131], 0, s[20:21]
	v_cndmask_b32_e32 v135, v135, v137, vcc
	v_cndmask_b32_e32 v134, v134, v136, vcc
	v_lshl_add_u64 v[134:135], v[134:135], 0, v[146:147]
	v_cndmask_b32_e64 v165, v135, v163, s[2:3]
	v_cndmask_b32_e64 v164, v134, v162, s[2:3]
	global_load_dwordx4 v[142:145], v[132:133], off
	global_load_dwordx4 v[138:141], v[130:131], off offset:64
	global_load_dwordx4 v[134:137], v[130:131], off offset:512
	s_nop 0
	global_load_dwordx4 v[130:133], v[130:131], off offset:576
	s_mov_b64 s[20:21], 0x20000
	v_lshl_add_u64 v[166:167], v[164:165], 0, s[20:21]
	v_lshl_add_u64 v[180:181], v[162:163], 0, s[20:21]
	s_mov_b64 s[20:21], 0x40000
	v_lshl_add_u64 v[168:169], v[164:165], 0, s[20:21]
	v_lshl_add_u64 v[182:183], v[162:163], 0, s[20:21]
	global_load_dwordx4 v[194:197], v[164:165], off
	global_load_dwordx4 v[198:201], v[164:165], off offset:64
	global_load_dwordx4 v[202:205], v[164:165], off offset:512
	global_load_dwordx4 v[206:209], v[164:165], off offset:576
	global_load_dwordx4 v[210:213], v[166:167], off
	global_load_dwordx4 v[218:221], v[166:167], off offset:64
	global_load_dwordx4 v[222:225], v[166:167], off offset:512
	global_load_dwordx4 v[226:229], v[166:167], off offset:576
	global_load_dwordx4 v[230:233], v[168:169], off
	global_load_dwordx4 v[234:237], v[168:169], off offset:64
	global_load_dwordx4 v[238:241], v[168:169], off offset:512
	global_load_dwordx4 v[242:245], v[168:169], off offset:576
	s_mov_b64 s[20:21], 0x60000
	v_lshl_add_u64 v[170:171], v[164:165], 0, s[20:21]
	v_lshl_add_u64 v[184:185], v[162:163], 0, s[20:21]
	s_mov_b64 s[20:21], 0x100000
	v_lshl_add_u64 v[172:173], v[164:165], 0, s[20:21]
	v_lshl_add_u64 v[186:187], v[162:163], 0, s[20:21]
	s_mov_b64 s[20:21], 0x120000
	v_lshl_add_u64 v[174:175], v[164:165], 0, s[20:21]
	v_lshl_add_u64 v[188:189], v[162:163], 0, s[20:21]
	s_mov_b64 s[20:21], 0x140000
	v_lshl_add_u64 v[176:177], v[164:165], 0, s[20:21]
	v_lshl_add_u64 v[190:191], v[162:163], 0, s[20:21]
	s_mov_b64 s[20:21], 0x160000
	v_lshl_add_u64 v[178:179], v[164:165], 0, s[20:21]
	v_lshl_add_u64 v[192:193], v[162:163], 0, s[20:21]
	s_waitcnt vmcnt(11)
	v_pk_fma_f32 v[128:129], v[128:129], v[144:145], v[196:197]
	v_pk_fma_f32 v[126:127], v[126:127], v[142:143], v[194:195]
	global_store_dwordx4 v[162:163], v[126:129], off
	global_load_dwordx4 v[194:197], v[170:171], off
	s_waitcnt vmcnt(12)
	v_pk_fma_f32 v[124:125], v[124:125], v[140:141], v[200:201]
	v_pk_fma_f32 v[122:123], v[122:123], v[138:139], v[198:199]
	global_store_dwordx4 v[162:163], v[122:125], off offset:64
	global_load_dwordx4 v[198:201], v[170:171], off offset:64
	s_waitcnt vmcnt(13)
	v_pk_fma_f32 v[120:121], v[120:121], v[136:137], v[204:205]
	v_pk_fma_f32 v[118:119], v[118:119], v[134:135], v[202:203]
	global_store_dwordx4 v[162:163], v[118:121], off offset:512
	global_load_dwordx4 v[202:205], v[170:171], off offset:512
	s_waitcnt vmcnt(14)
	v_pk_fma_f32 v[108:109], v[108:109], v[132:133], v[208:209]
	v_pk_fma_f32 v[106:107], v[106:107], v[130:131], v[206:207]
	global_store_dwordx4 v[162:163], v[106:109], off offset:576
	global_load_dwordx4 v[206:209], v[170:171], off offset:576
	s_waitcnt vmcnt(15)
	v_pk_fma_f32 v[116:117], v[116:117], v[144:145], v[212:213]
	v_pk_fma_f32 v[114:115], v[114:115], v[142:143], v[210:211]
	global_store_dwordx4 v[180:181], v[114:117], off
	global_load_dwordx4 v[210:213], v[172:173], off
	s_waitcnt vmcnt(16)
	v_pk_fma_f32 v[112:113], v[112:113], v[140:141], v[220:221]
	v_pk_fma_f32 v[110:111], v[110:111], v[138:139], v[218:219]
	global_store_dwordx4 v[180:181], v[110:113], off offset:64
	global_load_dwordx4 v[218:221], v[172:173], off offset:64
	s_waitcnt vmcnt(17)
	v_pk_fma_f32 v[104:105], v[104:105], v[136:137], v[224:225]
	v_pk_fma_f32 v[102:103], v[102:103], v[134:135], v[222:223]
	global_store_dwordx4 v[180:181], v[102:105], off offset:512
	global_load_dwordx4 v[222:225], v[172:173], off offset:512
	s_waitcnt vmcnt(18)
	v_pk_fma_f32 v[90:91], v[90:91], v[132:133], v[228:229]
	v_pk_fma_f32 v[88:89], v[88:89], v[130:131], v[226:227]
	global_store_dwordx4 v[180:181], v[88:91], off offset:576
	global_load_dwordx4 v[226:229], v[172:173], off offset:576
	s_waitcnt vmcnt(19)
	v_pk_fma_f32 v[100:101], v[100:101], v[144:145], v[232:233]
	v_pk_fma_f32 v[98:99], v[98:99], v[142:143], v[230:231]
	global_store_dwordx4 v[182:183], v[98:101], off
	global_load_dwordx4 v[230:233], v[174:175], off
	s_waitcnt vmcnt(20)
	v_pk_fma_f32 v[94:95], v[94:95], v[140:141], v[236:237]
	v_pk_fma_f32 v[92:93], v[92:93], v[138:139], v[234:235]
	global_store_dwordx4 v[182:183], v[92:95], off offset:64
	global_load_dwordx4 v[234:237], v[174:175], off offset:64
	s_waitcnt vmcnt(21)
	v_pk_fma_f32 v[86:87], v[86:87], v[136:137], v[240:241]
	v_pk_fma_f32 v[84:85], v[84:85], v[134:135], v[238:239]
	global_store_dwordx4 v[182:183], v[84:87], off offset:512
	global_load_dwordx4 v[238:241], v[174:175], off offset:512
	s_waitcnt vmcnt(22)
	v_pk_fma_f32 v[74:75], v[74:75], v[132:133], v[244:245]
	v_pk_fma_f32 v[72:73], v[72:73], v[130:131], v[242:243]
	global_store_dwordx4 v[182:183], v[72:75], off offset:576
	global_load_dwordx4 v[242:245], v[174:175], off offset:576
	s_waitcnt vmcnt(22)
	v_pk_fma_f32 v[82:83], v[82:83], v[144:145], v[196:197]
	v_pk_fma_f32 v[80:81], v[80:81], v[142:143], v[194:195]
	global_store_dwordx4 v[184:185], v[80:83], off
	global_load_dwordx4 v[194:197], v[176:177], off
	s_waitcnt vmcnt(22)
	v_pk_fma_f32 v[78:79], v[78:79], v[140:141], v[200:201]
	v_pk_fma_f32 v[76:77], v[76:77], v[138:139], v[198:199]
	global_store_dwordx4 v[184:185], v[76:79], off offset:64
	global_load_dwordx4 v[198:201], v[176:177], off offset:64
	s_waitcnt vmcnt(22)
	v_pk_fma_f32 v[70:71], v[70:71], v[136:137], v[204:205]
	v_pk_fma_f32 v[68:69], v[68:69], v[134:135], v[202:203]
	global_store_dwordx4 v[184:185], v[68:71], off offset:512
	global_load_dwordx4 v[202:205], v[176:177], off offset:512
	s_waitcnt vmcnt(22)
	v_pk_fma_f32 v[62:63], v[62:63], v[132:133], v[208:209]
	v_pk_fma_f32 v[60:61], v[60:61], v[130:131], v[206:207]
	global_store_dwordx4 v[184:185], v[60:63], off offset:576
	global_load_dwordx4 v[206:209], v[176:177], off offset:576
	s_waitcnt vmcnt(22)
	v_pk_fma_f32 v[66:67], v[66:67], v[144:145], v[212:213]
	v_pk_fma_f32 v[64:65], v[64:65], v[142:143], v[210:211]
	global_store_dwordx4 v[186:187], v[64:67], off
	global_load_dwordx4 v[210:213], v[178:179], off
	s_waitcnt vmcnt(22)
	v_pk_fma_f32 v[58:59], v[58:59], v[140:141], v[220:221]
	v_pk_fma_f32 v[56:57], v[56:57], v[138:139], v[218:219]
	global_store_dwordx4 v[186:187], v[56:59], off offset:64
	global_load_dwordx4 v[218:221], v[178:179], off offset:64
	s_waitcnt vmcnt(22)
	v_pk_fma_f32 v[54:55], v[54:55], v[136:137], v[224:225]
	v_pk_fma_f32 v[52:53], v[52:53], v[134:135], v[222:223]
	global_store_dwordx4 v[186:187], v[52:55], off offset:512
	global_load_dwordx4 v[222:225], v[178:179], off offset:512
	s_waitcnt vmcnt(22)
	v_pk_fma_f32 v[42:43], v[42:43], v[132:133], v[228:229]
	v_pk_fma_f32 v[40:41], v[40:41], v[130:131], v[226:227]
	global_store_dwordx4 v[186:187], v[40:43], off offset:576
	global_load_dwordx4 v[226:229], v[178:179], off offset:576
	s_waitcnt vmcnt(22)
	v_pk_fma_f32 v[50:51], v[50:51], v[144:145], v[232:233]
	v_pk_fma_f32 v[48:49], v[48:49], v[142:143], v[230:231]
	global_store_dwordx4 v[188:189], v[48:51], off
	s_waitcnt vmcnt(21)
	v_pk_fma_f32 v[46:47], v[46:47], v[140:141], v[236:237]
	v_pk_fma_f32 v[44:45], v[44:45], v[138:139], v[234:235]
	global_store_dwordx4 v[188:189], v[44:47], off offset:64
	s_waitcnt vmcnt(20)
	v_pk_fma_f32 v[38:39], v[38:39], v[136:137], v[240:241]
	v_pk_fma_f32 v[36:37], v[36:37], v[134:135], v[238:239]
	global_store_dwordx4 v[188:189], v[36:39], off offset:512
	s_waitcnt vmcnt(19)
	v_pk_fma_f32 v[26:27], v[26:27], v[132:133], v[244:245]
	v_pk_fma_f32 v[24:25], v[24:25], v[130:131], v[242:243]
	global_store_dwordx4 v[188:189], v[24:27], off offset:576
	s_waitcnt vmcnt(18)
	v_pk_fma_f32 v[34:35], v[34:35], v[144:145], v[196:197]
	v_pk_fma_f32 v[32:33], v[32:33], v[142:143], v[194:195]
	global_store_dwordx4 v[190:191], v[32:35], off
	s_waitcnt vmcnt(17)
	v_pk_fma_f32 v[30:31], v[30:31], v[140:141], v[200:201]
	v_pk_fma_f32 v[28:29], v[28:29], v[138:139], v[198:199]
	global_store_dwordx4 v[190:191], v[28:31], off offset:64
	s_waitcnt vmcnt(16)
	v_pk_fma_f32 v[22:23], v[22:23], v[136:137], v[204:205]
	v_pk_fma_f32 v[20:21], v[20:21], v[134:135], v[202:203]
	global_store_dwordx4 v[190:191], v[20:23], off offset:512
	s_waitcnt vmcnt(15)
	v_pk_fma_f32 v[10:11], v[10:11], v[132:133], v[208:209]
	v_pk_fma_f32 v[8:9], v[8:9], v[130:131], v[206:207]
	global_store_dwordx4 v[190:191], v[8:11], off offset:576
	s_waitcnt vmcnt(14)
	v_pk_fma_f32 v[18:19], v[18:19], v[144:145], v[212:213]
	v_pk_fma_f32 v[16:17], v[16:17], v[142:143], v[210:211]
	global_store_dwordx4 v[192:193], v[16:19], off
	s_waitcnt vmcnt(13)
	v_pk_fma_f32 v[14:15], v[14:15], v[140:141], v[220:221]
	v_pk_fma_f32 v[12:13], v[12:13], v[138:139], v[218:219]
	global_store_dwordx4 v[192:193], v[12:15], off offset:64
	s_waitcnt vmcnt(12)
	v_pk_fma_f32 v[6:7], v[6:7], v[136:137], v[224:225]
	v_pk_fma_f32 v[4:5], v[4:5], v[134:135], v[222:223]
	global_store_dwordx4 v[192:193], v[4:7], off offset:512
	s_waitcnt vmcnt(11)
	v_pk_fma_f32 v[2:3], v[2:3], v[132:133], v[228:229]
	v_pk_fma_f32 v[0:1], v[0:1], v[130:131], v[226:227]
	global_store_dwordx4 v[192:193], v[0:3], off offset:576
	s_mov_b64 s[20:21], -1
	s_cmp_eq_u32 s39, s42
	s_cbranch_scc1 .LBB0_1366
	s_andn2_b64 vcc, exec, s[6:7]
	s_cbranch_vccnz .LBB0_1365
	s_barrier
	s_branch .LBB0_1365
